# v18 plus scan_s3 forward loads hoisted above the carry loops and FFN2 gate loads ahead of the next-unit prefetch
# baseline (speedup 1.0000x reference)
; #define LAS __attribute__((address_space(3)))
; template <bool FP8>
; __device__ __forceinline__ void gemm_phase(LAS unsigned char* lds, const Desc& prob) {
;     ...
;         if (FP8 && has_next && prob.kind != K_PLE) {
;             const char* nb = nxt.b + (size_t)((cur.pm & 7) * 32) * prob.ldb;
;             __builtin_amdgcn_global_load_lds((const unsigned*)(nb + (size_t)tid * 128), (LAS unsigned*)(lds + 141312 + wid * 256), 4, 0, 0);
;         }
.LBB0_739:
	s_cmp_eq_u32 s1, 7
	s_cbranch_scc1 .LBB0_741
	s_and_b64 s[6:7], s[52:53], s[82:83]
	s_andn2_b64 vcc, exec, s[6:7]
	s_cbranch_vccnz .LBB0_741
	s_lshl_b32 s6, s36, 5
	s_and_b32 s6, s6, 0xe0
	v_mov_b32_e32 v2, s58
	v_mul_u32_u24_e32 v66, s6, v2
	v_lshl_add_u64 v[2:3], s[78:79], 0, v[66:67]
	v_lshl_add_u64 v[2:3], v[2:3], 0, v[214:215]
	s_mov_b32 m0, s96
	s_nop 0
	global_load_lds_dword v[2:3], off

; #define LAS __attribute__((address_space(3)))
; template <bool FP8>
; __device__ __forceinline__ void gemm_phase(LAS unsigned char* lds, const Desc& prob) {
;     ...
;         if (FP8 && has_next && prob.kind != K_PLE) {
;             const char* nb = nxt.b + (size_t)((cur.pm & 7) * 32) * prob.ldb;
;             __builtin_amdgcn_global_load_lds((const unsigned*)(nb + (size_t)tid * 128), (LAS unsigned*)(lds + 141312 + wid * 256), 4, 0, 0);
;         }
.LBB0_762:
	s_andn2_b64 vcc, exec, s[6:7]
	s_cbranch_vccnz .LBB0_764
	v_lshl_add_u32 v2, s36, 8, v48
	s_waitcnt lgkmcnt(0)
	v_ashrrev_i32_e32 v3, 31, v2
	v_lshlrev_b64 v[4:5], 10, v[2:3]
	v_lshl_add_u64 v[2:3], v[2:3], 2, s[54:55]
	global_load_dword v7, v[2:3], off offset:704
	global_load_dword v6, v[2:3], off offset:640
	global_load_dword v8, v[2:3], off offset:576
	global_load_dword v9, v[2:3], off offset:512
	global_load_dword v10, v[2:3], off offset:192
	global_load_dword v11, v[2:3], off offset:128
	global_load_dword v12, v[2:3], off offset:64
	s_nop 0
	global_load_dword v2, v[2:3], off
	s_and_b64 s[6:7], s[52:53], s[82:83]
	s_andn2_b64 vcc, exec, s[6:7]
	s_cbranch_vccnz .Lf2pf_skip
	s_lshl_b32 s6, s36, 5
	s_and_b32 s6, s6, 0xe0
	v_mov_b32_e32 v14, s58
	v_mul_u32_u24_e32 v66, s6, v14
	v_lshl_add_u64 v[14:15], s[78:79], 0, v[66:67]
	v_lshl_add_u64 v[14:15], v[14:15], 0, v[214:215]
	s_mov_b32 m0, s96
	s_nop 0
	global_load_lds_dword v[14:15], off
.Lf2pf_skip:
	s_lshl_b32 s6, s44, 8
	s_ashr_i32 s7, s6, 31
	v_lshl_add_u64 v[4:5], s[50:51], 0, v[4:5]
	v_mov_b32_e32 v35, v67
	v_lshl_add_u64 v[4:5], v[4:5], 0, s[6:7]
	v_lshl_add_u64 v[4:5], v[4:5], 0, v[34:35]
	v_bfe_u32 v13, v238, 4, 1
	v_mul_u32_u24_e32 v13, 0x78, v13
	v_add_co_u32_e32 v4, vcc, v4, v13
	s_nop 1
	v_addc_co_u32_e32 v5, vcc, 0, v5, vcc
	s_and_b64 vcc, s[52:53], s[82:83]
	s_cbranch_vccz .Lf2pf_w0
	s_waitcnt vmcnt(1)
	s_branch .Lf2pf_wd

.Lf2pf_wd:
	s_nop 0
	v_mul_f32_e32 v52, 0x42800000, v2
	v_mul_f32_e32 v54, 0x42800000, v12
	v_mul_f32_e32 v56, 0x42800000, v11
	v_mul_f32_e32 v58, 0x42800000, v10
	v_mul_f32_e32 v60, 0x42800000, v9
	v_mul_f32_e32 v62, 0x42800000, v8
	v_mul_f32_e32 v64, 0x42800000, v6
	v_mul_f32_e32 v16, 0x42800000, v7
	v_pk_mul_f32 v[36:37], v[72:73], v[52:53] op_sel_hi:[1,0]
	v_pk_mul_f32 v[38:39], v[74:75], v[52:53] op_sel_hi:[1,0]
	v_pk_mul_f32 v[40:41], v[192:193], v[52:53] op_sel_hi:[1,0]
	v_pk_mul_f32 v[42:43], v[194:195], v[52:53] op_sel_hi:[1,0]
	v_pk_mul_f32 v[44:45], v[164:165], v[52:53] op_sel_hi:[1,0]
	v_pk_mul_f32 v[46:47], v[166:167], v[52:53] op_sel_hi:[1,0]
	v_pk_mul_f32 v[48:49], v[160:161], v[52:53] op_sel_hi:[1,0]
	v_pk_mul_f32 v[50:51], v[162:163], v[52:53] op_sel_hi:[1,0]
	v_med3_f32 v36, v36, s19, v248
	v_med3_f32 v37, v37, s19, v248
	v_med3_f32 v38, v38, s19, v248
	v_med3_f32 v39, v39, s19, v248
	v_med3_f32 v40, v40, s19, v248
	v_med3_f32 v41, v41, s19, v248
	v_med3_f32 v42, v42, s19, v248
	v_med3_f32 v43, v43, s19, v248
	v_med3_f32 v44, v44, s19, v248
	v_med3_f32 v45, v45, s19, v248
	v_med3_f32 v46, v46, s19, v248
	v_med3_f32 v47, v47, s19, v248
	v_med3_f32 v48, v48, s19, v248
	v_med3_f32 v49, v49, s19, v248
	v_med3_f32 v50, v50, s19, v248
	v_med3_f32 v51, v51, s19, v248
	v_cvt_pk_fp8_f32 v20, v36, v37
	v_cvt_pk_fp8_f32 v21, v40, v41
	v_cvt_pk_fp8_f32 v22, v44, v45
	v_cvt_pk_fp8_f32 v23, v48, v49
	v_cvt_pk_fp8_f32 v20, v38, v39 op_sel:[0,0,1]
	v_cvt_pk_fp8_f32 v21, v42, v43 op_sel:[0,0,1]
	v_cvt_pk_fp8_f32 v22, v46, v47 op_sel:[0,0,1]
	v_cvt_pk_fp8_f32 v23, v50, v51 op_sel:[0,0,1]
	s_nop 1
	v_permlane16_swap_b32_e32 v20, v22
	v_permlane16_swap_b32_e32 v21, v23
	global_store_dwordx4 v[4:5], v[20:23], off
	v_pk_mul_f32 v[36:37], v[188:189], v[54:55] op_sel_hi:[1,0]
	v_pk_mul_f32 v[38:39], v[190:191], v[54:55] op_sel_hi:[1,0]
	v_pk_mul_f32 v[40:41], v[184:185], v[54:55] op_sel_hi:[1,0]
	v_pk_mul_f32 v[42:43], v[186:187], v[54:55] op_sel_hi:[1,0]
	v_pk_mul_f32 v[44:45], v[156:157], v[54:55] op_sel_hi:[1,0]
	v_pk_mul_f32 v[46:47], v[158:159], v[54:55] op_sel_hi:[1,0]
	v_pk_mul_f32 v[48:49], v[152:153], v[54:55] op_sel_hi:[1,0]
	v_pk_mul_f32 v[50:51], v[154:155], v[54:55] op_sel_hi:[1,0]
	v_med3_f32 v36, v36, s19, v248
	v_med3_f32 v37, v37, s19, v248
	v_med3_f32 v38, v38, s19, v248
	v_med3_f32 v39, v39, s19, v248
	v_med3_f32 v40, v40, s19, v248
	v_med3_f32 v41, v41, s19, v248
	v_med3_f32 v42, v42, s19, v248
	v_med3_f32 v43, v43, s19, v248
	v_med3_f32 v44, v44, s19, v248
	v_med3_f32 v45, v45, s19, v248
	v_med3_f32 v46, v46, s19, v248
	v_med3_f32 v47, v47, s19, v248
	v_med3_f32 v48, v48, s19, v248
	v_med3_f32 v49, v49, s19, v248
	v_med3_f32 v50, v50, s19, v248
	v_med3_f32 v51, v51, s19, v248
	v_cvt_pk_fp8_f32 v28, v36, v37
	v_cvt_pk_fp8_f32 v29, v40, v41
	v_cvt_pk_fp8_f32 v30, v44, v45
	v_cvt_pk_fp8_f32 v31, v48, v49
	v_cvt_pk_fp8_f32 v28, v38, v39 op_sel:[0,0,1]
	v_cvt_pk_fp8_f32 v29, v42, v43 op_sel:[0,0,1]
	v_cvt_pk_fp8_f32 v30, v46, v47 op_sel:[0,0,1]
	v_cvt_pk_fp8_f32 v31, v50, v51 op_sel:[0,0,1]
	v_add_co_u32_e32 v14, vcc, 0x4000, v4
	s_nop 1
	v_addc_co_u32_e32 v15, vcc, 0, v5, vcc
	v_permlane16_swap_b32_e32 v28, v30
	v_permlane16_swap_b32_e32 v29, v31
	global_store_dwordx4 v[14:15], v[28:31], off
	v_pk_mul_f32 v[36:37], v[180:181], v[56:57] op_sel_hi:[1,0]
	v_pk_mul_f32 v[38:39], v[182:183], v[56:57] op_sel_hi:[1,0]
	v_pk_mul_f32 v[40:41], v[176:177], v[56:57] op_sel_hi:[1,0]
	v_pk_mul_f32 v[42:43], v[178:179], v[56:57] op_sel_hi:[1,0]
	v_pk_mul_f32 v[44:45], v[148:149], v[56:57] op_sel_hi:[1,0]
	v_pk_mul_f32 v[46:47], v[150:151], v[56:57] op_sel_hi:[1,0]
	v_pk_mul_f32 v[48:49], v[144:145], v[56:57] op_sel_hi:[1,0]
	v_pk_mul_f32 v[50:51], v[146:147], v[56:57] op_sel_hi:[1,0]
	v_med3_f32 v36, v36, s19, v248
	v_med3_f32 v37, v37, s19, v248
	v_med3_f32 v38, v38, s19, v248
	v_med3_f32 v39, v39, s19, v248
	v_med3_f32 v40, v40, s19, v248
	v_med3_f32 v41, v41, s19, v248
	v_med3_f32 v42, v42, s19, v248
	v_med3_f32 v43, v43, s19, v248
	v_med3_f32 v44, v44, s19, v248
	v_med3_f32 v45, v45, s19, v248
	v_med3_f32 v46, v46, s19, v248
	v_med3_f32 v47, v47, s19, v248
	v_med3_f32 v48, v48, s19, v248
	v_med3_f32 v49, v49, s19, v248
	v_med3_f32 v50, v50, s19, v248
	v_med3_f32 v51, v51, s19, v248
	v_cvt_pk_fp8_f32 v20, v36, v37
	v_cvt_pk_fp8_f32 v21, v40, v41
	v_cvt_pk_fp8_f32 v22, v44, v45
	v_cvt_pk_fp8_f32 v23, v48, v49
	v_cvt_pk_fp8_f32 v20, v38, v39 op_sel:[0,0,1]
	v_cvt_pk_fp8_f32 v21, v42, v43 op_sel:[0,0,1]
	v_cvt_pk_fp8_f32 v22, v46, v47 op_sel:[0,0,1]
	v_cvt_pk_fp8_f32 v23, v50, v51 op_sel:[0,0,1]
	v_add_co_u32_e32 v14, vcc, 0x8000, v4
	s_nop 1
	v_addc_co_u32_e32 v15, vcc, 0, v5, vcc
	v_permlane16_swap_b32_e32 v20, v22
	v_permlane16_swap_b32_e32 v21, v23
	global_store_dwordx4 v[14:15], v[20:23], off
	v_pk_mul_f32 v[36:37], v[172:173], v[58:59] op_sel_hi:[1,0]
	v_pk_mul_f32 v[38:39], v[174:175], v[58:59] op_sel_hi:[1,0]
	v_pk_mul_f32 v[40:41], v[168:169], v[58:59] op_sel_hi:[1,0]
	v_pk_mul_f32 v[42:43], v[170:171], v[58:59] op_sel_hi:[1,0]
	v_pk_mul_f32 v[44:45], v[140:141], v[58:59] op_sel_hi:[1,0]
	v_pk_mul_f32 v[46:47], v[142:143], v[58:59] op_sel_hi:[1,0]
	v_pk_mul_f32 v[48:49], v[136:137], v[58:59] op_sel_hi:[1,0]
	v_pk_mul_f32 v[50:51], v[138:139], v[58:59] op_sel_hi:[1,0]
	v_med3_f32 v36, v36, s19, v248
	v_med3_f32 v37, v37, s19, v248
	v_med3_f32 v38, v38, s19, v248
	v_med3_f32 v39, v39, s19, v248
	v_med3_f32 v40, v40, s19, v248
	v_med3_f32 v41, v41, s19, v248
	v_med3_f32 v42, v42, s19, v248
	v_med3_f32 v43, v43, s19, v248
	v_med3_f32 v44, v44, s19, v248
	v_med3_f32 v45, v45, s19, v248
	v_med3_f32 v46, v46, s19, v248
	v_med3_f32 v47, v47, s19, v248
	v_med3_f32 v48, v48, s19, v248
	v_med3_f32 v49, v49, s19, v248
	v_med3_f32 v50, v50, s19, v248
	v_med3_f32 v51, v51, s19, v248
	v_cvt_pk_fp8_f32 v28, v36, v37
	v_cvt_pk_fp8_f32 v29, v40, v41
	v_cvt_pk_fp8_f32 v30, v44, v45
	v_cvt_pk_fp8_f32 v31, v48, v49
	v_cvt_pk_fp8_f32 v28, v38, v39 op_sel:[0,0,1]
	v_cvt_pk_fp8_f32 v29, v42, v43 op_sel:[0,0,1]
	v_cvt_pk_fp8_f32 v30, v46, v47 op_sel:[0,0,1]
	v_cvt_pk_fp8_f32 v31, v50, v51 op_sel:[0,0,1]
	v_add_co_u32_e32 v14, vcc, 0xc000, v4
	s_nop 1
	v_addc_co_u32_e32 v15, vcc, 0, v5, vcc
	v_permlane16_swap_b32_e32 v28, v30
	v_permlane16_swap_b32_e32 v29, v31
	global_store_dwordx4 v[14:15], v[28:31], off
	v_pk_mul_f32 v[36:37], v[132:133], v[60:61] op_sel_hi:[1,0]
	v_pk_mul_f32 v[38:39], v[134:135], v[60:61] op_sel_hi:[1,0]
	v_pk_mul_f32 v[40:41], v[128:129], v[60:61] op_sel_hi:[1,0]
	v_pk_mul_f32 v[42:43], v[130:131], v[60:61] op_sel_hi:[1,0]
	v_pk_mul_f32 v[44:45], v[100:101], v[60:61] op_sel_hi:[1,0]
	v_pk_mul_f32 v[46:47], v[102:103], v[60:61] op_sel_hi:[1,0]
	v_pk_mul_f32 v[48:49], v[96:97], v[60:61] op_sel_hi:[1,0]
	v_pk_mul_f32 v[50:51], v[98:99], v[60:61] op_sel_hi:[1,0]
	v_med3_f32 v36, v36, s19, v248
	v_med3_f32 v37, v37, s19, v248
	v_med3_f32 v38, v38, s19, v248
	v_med3_f32 v39, v39, s19, v248
	v_med3_f32 v40, v40, s19, v248
	v_med3_f32 v41, v41, s19, v248
	v_med3_f32 v42, v42, s19, v248
	v_med3_f32 v43, v43, s19, v248
	v_med3_f32 v44, v44, s19, v248
	v_med3_f32 v45, v45, s19, v248
	v_med3_f32 v46, v46, s19, v248
	v_med3_f32 v47, v47, s19, v248
	v_med3_f32 v48, v48, s19, v248
	v_med3_f32 v49, v49, s19, v248
	v_med3_f32 v50, v50, s19, v248
	v_med3_f32 v51, v51, s19, v248
	v_cvt_pk_fp8_f32 v20, v36, v37
	v_cvt_pk_fp8_f32 v21, v40, v41
	v_cvt_pk_fp8_f32 v22, v44, v45
	v_cvt_pk_fp8_f32 v23, v48, v49
	v_cvt_pk_fp8_f32 v20, v38, v39 op_sel:[0,0,1]
	v_cvt_pk_fp8_f32 v21, v42, v43 op_sel:[0,0,1]
	v_cvt_pk_fp8_f32 v22, v46, v47 op_sel:[0,0,1]
	v_cvt_pk_fp8_f32 v23, v50, v51 op_sel:[0,0,1]
	v_add_co_u32_e32 v14, vcc, 0x20000, v4
	s_nop 1
	v_addc_co_u32_e32 v15, vcc, 0, v5, vcc
	v_permlane16_swap_b32_e32 v20, v22
	v_permlane16_swap_b32_e32 v21, v23
	global_store_dwordx4 v[14:15], v[20:23], off
	v_pk_mul_f32 v[36:37], v[124:125], v[62:63] op_sel_hi:[1,0]
	v_pk_mul_f32 v[38:39], v[126:127], v[62:63] op_sel_hi:[1,0]
	v_pk_mul_f32 v[40:41], v[120:121], v[62:63] op_sel_hi:[1,0]
	v_pk_mul_f32 v[42:43], v[122:123], v[62:63] op_sel_hi:[1,0]
	v_pk_mul_f32 v[44:45], v[92:93], v[62:63] op_sel_hi:[1,0]
	v_pk_mul_f32 v[46:47], v[94:95], v[62:63] op_sel_hi:[1,0]
	v_pk_mul_f32 v[48:49], v[88:89], v[62:63] op_sel_hi:[1,0]
	v_pk_mul_f32 v[50:51], v[90:91], v[62:63] op_sel_hi:[1,0]
	v_med3_f32 v36, v36, s19, v248
	v_med3_f32 v37, v37, s19, v248
	v_med3_f32 v38, v38, s19, v248
	v_med3_f32 v39, v39, s19, v248
	v_med3_f32 v40, v40, s19, v248
	v_med3_f32 v41, v41, s19, v248
	v_med3_f32 v42, v42, s19, v248
	v_med3_f32 v43, v43, s19, v248
	v_med3_f32 v44, v44, s19, v248
	v_med3_f32 v45, v45, s19, v248
	v_med3_f32 v46, v46, s19, v248
	v_med3_f32 v47, v47, s19, v248
	v_med3_f32 v48, v48, s19, v248
	v_med3_f32 v49, v49, s19, v248
	v_med3_f32 v50, v50, s19, v248
	v_med3_f32 v51, v51, s19, v248
	v_cvt_pk_fp8_f32 v28, v36, v37
	v_cvt_pk_fp8_f32 v29, v40, v41
	v_cvt_pk_fp8_f32 v30, v44, v45
	v_cvt_pk_fp8_f32 v31, v48, v49
	v_cvt_pk_fp8_f32 v28, v38, v39 op_sel:[0,0,1]
	v_cvt_pk_fp8_f32 v29, v42, v43 op_sel:[0,0,1]
	v_cvt_pk_fp8_f32 v30, v46, v47 op_sel:[0,0,1]
	v_cvt_pk_fp8_f32 v31, v50, v51 op_sel:[0,0,1]
	v_add_co_u32_e32 v14, vcc, 0x24000, v4
	s_nop 1
	v_addc_co_u32_e32 v15, vcc, 0, v5, vcc
	v_permlane16_swap_b32_e32 v28, v30
	v_permlane16_swap_b32_e32 v29, v31
	global_store_dwordx4 v[14:15], v[28:31], off
	v_pk_mul_f32 v[36:37], v[116:117], v[64:65] op_sel_hi:[1,0]
	v_pk_mul_f32 v[38:39], v[118:119], v[64:65] op_sel_hi:[1,0]
	v_pk_mul_f32 v[40:41], v[112:113], v[64:65] op_sel_hi:[1,0]
	v_pk_mul_f32 v[42:43], v[114:115], v[64:65] op_sel_hi:[1,0]
	v_pk_mul_f32 v[44:45], v[84:85], v[64:65] op_sel_hi:[1,0]
	v_pk_mul_f32 v[46:47], v[86:87], v[64:65] op_sel_hi:[1,0]
	v_pk_mul_f32 v[48:49], v[80:81], v[64:65] op_sel_hi:[1,0]
	v_pk_mul_f32 v[50:51], v[82:83], v[64:65] op_sel_hi:[1,0]
	v_med3_f32 v36, v36, s19, v248
	v_med3_f32 v37, v37, s19, v248
	v_med3_f32 v38, v38, s19, v248
	v_med3_f32 v39, v39, s19, v248
	v_med3_f32 v40, v40, s19, v248
	v_med3_f32 v41, v41, s19, v248
	v_med3_f32 v42, v42, s19, v248
	v_med3_f32 v43, v43, s19, v248
	v_med3_f32 v44, v44, s19, v248
	v_med3_f32 v45, v45, s19, v248
	v_med3_f32 v46, v46, s19, v248
	v_med3_f32 v47, v47, s19, v248
	v_med3_f32 v48, v48, s19, v248
	v_med3_f32 v49, v49, s19, v248
	v_med3_f32 v50, v50, s19, v248
	v_med3_f32 v51, v51, s19, v248
	v_cvt_pk_fp8_f32 v20, v36, v37
	v_cvt_pk_fp8_f32 v21, v40, v41
	v_cvt_pk_fp8_f32 v22, v44, v45
	v_cvt_pk_fp8_f32 v23, v48, v49
	v_cvt_pk_fp8_f32 v20, v38, v39 op_sel:[0,0,1]
	v_cvt_pk_fp8_f32 v21, v42, v43 op_sel:[0,0,1]
	v_cvt_pk_fp8_f32 v22, v46, v47 op_sel:[0,0,1]
	v_cvt_pk_fp8_f32 v23, v50, v51 op_sel:[0,0,1]
	v_add_co_u32_e32 v14, vcc, 0x28000, v4
	s_nop 1
	v_addc_co_u32_e32 v15, vcc, 0, v5, vcc
	v_permlane16_swap_b32_e32 v20, v22
	v_permlane16_swap_b32_e32 v21, v23
	global_store_dwordx4 v[14:15], v[20:23], off
	v_pk_mul_f32 v[36:37], v[108:109], v[16:17] op_sel_hi:[1,0]
	v_pk_mul_f32 v[38:39], v[110:111], v[16:17] op_sel_hi:[1,0]
	v_pk_mul_f32 v[40:41], v[104:105], v[16:17] op_sel_hi:[1,0]
	v_pk_mul_f32 v[42:43], v[106:107], v[16:17] op_sel_hi:[1,0]
	v_pk_mul_f32 v[44:45], v[76:77], v[16:17] op_sel_hi:[1,0]
	v_pk_mul_f32 v[46:47], v[78:79], v[16:17] op_sel_hi:[1,0]
	v_pk_mul_f32 v[48:49], v[68:69], v[16:17] op_sel_hi:[1,0]
	v_pk_mul_f32 v[50:51], v[70:71], v[16:17] op_sel_hi:[1,0]
	v_med3_f32 v36, v36, s19, v248
	v_med3_f32 v37, v37, s19, v248
	v_med3_f32 v38, v38, s19, v248
	v_med3_f32 v39, v39, s19, v248
	v_med3_f32 v40, v40, s19, v248
	v_med3_f32 v41, v41, s19, v248
	v_med3_f32 v42, v42, s19, v248
	v_med3_f32 v43, v43, s19, v248
	v_med3_f32 v44, v44, s19, v248
	v_med3_f32 v45, v45, s19, v248
	v_med3_f32 v46, v46, s19, v248
	v_med3_f32 v47, v47, s19, v248
	v_med3_f32 v48, v48, s19, v248
	v_med3_f32 v49, v49, s19, v248
	v_med3_f32 v50, v50, s19, v248
	v_med3_f32 v51, v51, s19, v248
	v_cvt_pk_fp8_f32 v28, v36, v37
	v_cvt_pk_fp8_f32 v29, v40, v41
	v_cvt_pk_fp8_f32 v30, v44, v45
	v_cvt_pk_fp8_f32 v31, v48, v49
	v_cvt_pk_fp8_f32 v28, v38, v39 op_sel:[0,0,1]
	v_cvt_pk_fp8_f32 v29, v42, v43 op_sel:[0,0,1]
	v_cvt_pk_fp8_f32 v30, v46, v47 op_sel:[0,0,1]
	v_cvt_pk_fp8_f32 v31, v50, v51 op_sel:[0,0,1]
	v_add_co_u32_e32 v14, vcc, 0x2c000, v4
	s_nop 1
	v_addc_co_u32_e32 v15, vcc, 0, v5, vcc
	v_permlane16_swap_b32_e32 v28, v30
	v_permlane16_swap_b32_e32 v29, v31
	global_store_dwordx4 v[14:15], v[28:31], off
